# grid barrier: XCD leader publishes the per-XCD generation before its own L1 invalidate
# speedup vs baseline: 1.0139x; 1.0041x over previous
.LBB0_221:
	s_or_b64 exec, exec, s[6:7]
	v_mov_b32_e32 v1, 0x2000
	v_mov_b32_e32 v2, 1
	s_waitcnt vmcnt(0)
	global_atomic_add v1, v2, s[4:5] offset:1024
	buffer_inv sc1
	s_waitcnt vmcnt(0)

.LBB0_279:
	s_or_b64 exec, exec, s[4:5]
	v_mov_b32_e32 v1, 0x2000
	v_mov_b32_e32 v2, 1
	s_waitcnt vmcnt(0)
	global_atomic_add v1, v2, s[2:3] offset:1024
	buffer_inv sc1
	s_waitcnt vmcnt(0)

.LBB0_3813:
	s_or_b64 exec, exec, s[8:9]
	v_mov_b32_e32 v1, 0x2000
	v_mov_b32_e32 v2, 1
	s_waitcnt vmcnt(0)
	global_atomic_add v1, v2, s[4:5] offset:1024
	buffer_inv sc1
	s_waitcnt vmcnt(0)
